# baseline (speedup 1.0000x reference)
.LBB1_3:
	v_mov_b32_e32 v156, v0
	s_nop 0
	v_ashrrev_i32_e32 v157, 31, v156
	v_and_b32_e32 v167, 63, v156
	v_lshl_add_u64 v[6:7], v[156:157], 3, s[10:11]
	v_lshlrev_b32_e32 v169, 3, v167
	v_readfirstlane_b32 s4, v156
	s_ashr_i32 s27, s4, 7
	s_lshl_b32 s0, s27, 1
	s_ashr_i32 s1, s0, 31
	s_lshl_b64 s[2:3], s[0:1], 13
	s_add_u32 s2, s8, s2
	s_addc_u32 s3, s9, s3
	s_add_u32 s28, s2, 0x18000
	s_addc_u32 s29, s3, 0
	v_lshlrev_b32_e32 v154, 4, v167
	v_lshl_add_u64 v[6:7], s[28:29], 0, v[154:155]
	v_or_b32_e32 v8, 0x800, v169
	v_add_co_u32_e32 v6, vcc, s23, v6
	v_lshlrev_b32_e32 v168, 1, v8
	s_nop 0
	v_addc_co_u32_e32 v7, vcc, 0, v7, vcc
	global_load_dwordx4 v[150:153], v154, s[28:29]
	global_load_dwordx4 v[146:149], v154, s[28:29] offset:1024
	global_load_dwordx4 v[142:145], v154, s[28:29] offset:2048
	global_load_dwordx4 v[138:141], v154, s[28:29] offset:3072
	global_load_dwordx4 v[126:129], v[6:7], off offset:1024
	global_load_dwordx4 v[122:125], v[6:7], off offset:2048
	global_load_dwordx4 v[134:137], v168, s[28:29]
	global_load_dwordx4 v[130:133], v[6:7], off offset:3072
	v_lshl_add_u64 v[6:7], s[2:3], 0, v[154:155]
	v_lshl_add_u64 v[8:9], v[6:7], 0, s[16:17]
	v_add_co_u32_e32 v6, vcc, 0x28000, v6
	s_nop 1
	v_addc_co_u32_e32 v7, vcc, 0, v7, vcc
	global_load_dwordx4 v[86:89], v[6:7], off
	global_load_dwordx4 v[82:85], v[8:9], off offset:1024
	v_lshrrev_b32_e32 v182, 5, v167
	s_ashr_i32 s2, s4, 6
	s_lshl_b32 s3, s2, 3
	s_and_b32 s5, s3, 8
	s_bfe_u32 s26, s2, 0x10001
	s_or_b32 s5, s26, s5
	s_lshl_b32 s26, s2, 9
	s_and_b32 s26, s26, 0x400
	s_lshl_b32 s5, s5, 4
	s_or_b32 s28, s5, s26
	v_bfe_u32 v76, v156, 4, 1
	v_bitop3_b32 v77, v182, v156, 1 bitop3:0x78
	v_lshlrev_b32_e32 v154, 2, v182
	v_xor_b32_e32 v77, v77, v76
	v_bitop3_b32 v78, v154, v156, 4 bitop3:0x78
	v_and_b32_e32 v79, 10, v156
	v_or3_b32 v77, v79, v78, v77
	s_lshl_b32 s5, s2, 4
	v_lshlrev_b32_e32 v77, 4, v77
	s_lshl_b32 s3, s2, 13
	s_and_b32 s29, s5, 16
	v_lshlrev_b32_e32 v170, 8, v182
	v_lshl_or_b32 v171, v76, 10, v77
	s_or_b32 s26, s29, s3
	v_bitop3_b32 v179, v171, s26, v170 bitop3:0x36
	s_or_b32 s5, s26, 0x280
	v_bitop3_b32 v178, v171, s5, v170 bitop3:0x36
	s_or_b32 s30, s3, 0x800
	s_or_b32 s33, s3, 0x1000
	s_or_b32 s29, s29, 64
	s_or_b32 s34, s29, s33
	v_bitop3_b32 v180, v171, s34, v170 bitop3:0x36
	s_or_b32 s29, s3, s29
	s_or_b32 s29, s29, 0x1280
	s_and_b32 s5, s2, 1
	s_lshl_b32 s31, s5, 4
	s_or_b32 s2, s31, s3
	v_bitop3_b32 v173, v171, s2, v170 bitop3:0x36
	v_bitop3_b32 v76, v156, 31, v156 bitop3:0xc
	v_lshrrev_b32_e32 v77, 4, v76
	v_bitop3_b32 v78, v76, v182, 1 bitop3:0x6c
	v_xor_b32_e32 v78, v78, v77
	v_bitop3_b32 v76, v76, v154, 4 bitop3:0x6c
	v_bitop3_b32 v79, v156, 10, 31 bitop3:8
	v_or3_b32 v76, v79, v76, v78
	v_lshlrev_b32_e32 v77, 10, v77
	v_lshlrev_b32_e32 v76, 4, v76
	v_or3_b32 v154, v77, v76, v170
	v_bitop3_b32 v172, s2, v154, v159 bitop3:0x36
	v_bitop3_b32 v176, v171, s29, v170 bitop3:0x36
	s_or_b32 s29, s31, s30
	s_or_b32 s29, s29, 0xa0
	v_bitop3_b32 v175, v171, s29, v170 bitop3:0x36
	s_or_b32 s29, s2, 0xaa0
	s_xor_b32 s29, s29, 0x80
	v_xor_b32_e32 v174, s29, v154
	s_or_b32 s29, s26, 0x18e0
	v_bitop3_b32 v181, v171, s29, v170 bitop3:0x36
	s_or_b32 s29, s26, 0x1a60
	v_bitop3_b32 v177, v171, s29, v170 bitop3:0x36
	s_or_b32 s29, s31, 64
	s_or_b32 s3, s3, s29
	s_mov_b32 s41, s3
	s_or_b32 s29, s29, s33
	s_mov_b32 s40, s29
	s_or_b32 s3, s2, 0x18e0
	s_mov_b32 s42, s3
	s_or_b32 s2, s2, 0x1ae0
	s_xor_b32 s2, s2, 0x80
	s_mov_b32 s43, s2
	v_lshl_add_u32 v166, v156, 2, v165
	s_cmp_lt_i32 s22, 0
	s_cbranch_scc0 .Lskip_stage0
	v_lshl_add_u32 v6, v156, 3, v1
	v_cmp_gt_i32_e32 vcc, 64, v156
	s_waitcnt vmcnt(19)
	ds_write_b64 v6, v[4:5]
	s_and_saveexec_b64 s[2:3], vcc
	s_cbranch_execz .LBB1_7
	s_waitcnt vmcnt(18)
	ds_write_b64 v6, v[2:3] offset:2048
